# sparse L0 tile loop: exp/convert block runs behind the V-fragment LDS reads; the next V tile's DMA is issued after those reads landed, right before the PV MFMAs
# baseline (speedup 1.0000x reference)
; #define SBAR() __builtin_amdgcn_sched_barrier(0)
; #define SBAR() __builtin_amdgcn_sched_barrier(0)
; #define D8_MX(a, b, c) __builtin_amdgcn_mfma_scale_f32_32x32x64_f8f6f4(a, b, c, 0, 0, 0, 0, 0, 0)
; template <class P>
; __device__ __forceinline__ void sparse8_wave(P& pol, LAS unsigned char* wll, int lane) {
;     ...
;         if constexpr (P::LSUM) {
; #pragma unroll
;             for (int r = 0; r < 16; ++r) { p0[r] = __builtin_amdgcn_exp2f(p0[r]); p1[r] = __builtin_amdgcn_exp2f(p1[r]); } }
;         else { float ps = 0.f;
; #pragma unroll
;             for (int r = 0; r < 16; ++r) { p0[r] = __builtin_amdgcn_exp2f(p0[r]); p1[r] = __builtin_amdgcn_exp2f(p1[r]); ps += p0[r] + p1[r]; }
;             { auto rr = __builtin_amdgcn_permlane32_swap(__float_as_uint(ps), __float_as_uint(ps), false, false);
;               ps = __uint_as_float(rr[0]) + __uint_as_float(rr[1]); }
;             l_reg = l_reg * alpha + ps; }
;         const i32x8 pa = (i32x8){(int)pk4_fp8(p0[0], p0[1], p0[2], p0[3]), (int)pk4_fp8(p0[4], p0[5], p0[6], p0[7]), (int)pk4_fp8(p0[8], p0[9], p0[10], p0[11]), (int)pk4_fp8(p0[12], p0[13], p0[14], p0[15]),
;                                  (int)pk4_fp8(p1[0], p1[1], p1[2], p1[3]), (int)pk4_fp8(p1[4], p1[5], p1[6], p1[7]), (int)pk4_fp8(p1[8], p1[9], p1[10], p1[11]), (int)pk4_fp8(p1[12], p1[13], p1[14], p1[15])};
;         SBAR();
;         if (more) asm volatile("s_waitcnt vmcnt(8)" ::: "memory"); else asm volatile("s_waitcnt vmcnt(0)" ::: "memory");
;         SBAR();
;         { i32x8 bfr[4];
; #pragma unroll
;           for (int d0 = 0; d0 < 4; ++d0) { const int c = 32 * d0 + r32; const char* vp = Vl + c * 64; const int sw = (c >> 2) & 3;
;             const i32x4 lo = *(const i32x4*)(vp + (((2 * hi) ^ sw) << 4)), hh = *(const i32x4*)(vp + (((2 * hi + 1) ^ sw) << 4)); bfr[d0] = __builtin_shufflevector(lo, hh, 0, 1, 2, 3, 4, 5, 6, 7); }
;           asm volatile("s_waitcnt lgkmcnt(0)" ::: "memory"); SBAR();
;           if (more) SP8_DMA_V(tn);
;           SBAR();
; #pragma unroll
;           for (int d0 = 0; d0 < 4; ++d0) o[d0] = D8_MX(pa, bfr[d0], o[d0]);
;           if constexpr (P::LSUM) lacc = D8_MX(pa, ones8, lacc); }
.LBB0_575:
	ds_read_b128 v[104:107], v180 offset:8192
	ds_read_b128 v[96:99], v180 offset:10240
	ds_read_b128 v[108:111], v181 offset:8192
	ds_read_b128 v[100:103], v181 offset:10240
	ds_read_b128 v[120:123], v180 offset:12288
	ds_read_b128 v[112:115], v180 offset:14336
	ds_read_b128 v[124:127], v181 offset:12288
	ds_read_b128 v[116:119], v181 offset:14336
	v_exp_f32_e32 v198, v145
	v_exp_f32_e32 v202, v147
	v_exp_f32_e32 v144, v144
	v_exp_f32_e32 v145, v146
	v_exp_f32_e32 v146, v149
	v_exp_f32_e32 v147, v151
	v_exp_f32_e32 v149, v150
	v_exp_f32_e32 v199, v153
	v_exp_f32_e32 v203, v155
	v_exp_f32_e32 v150, v152
	v_exp_f32_e32 v151, v154
	v_exp_f32_e32 v152, v157
	v_exp_f32_e32 v154, v156
	v_exp_f32_e32 v200, v185
	v_exp_f32_e32 v204, v187
	v_exp_f32_e32 v156, v184
	v_exp_f32_e32 v157, v186
	v_exp_f32_e32 v201, v193
	v_exp_f32_e32 v205, v195
	v_exp_f32_e32 v186, v192
	v_exp_f32_e32 v187, v194
	v_exp_f32_e32 v148, v148
	v_exp_f32_e32 v153, v159
	v_exp_f32_e32 v155, v158
	v_exp_f32_e32 v158, v189
	v_exp_f32_e32 v159, v191
	v_exp_f32_e32 v184, v188
	v_exp_f32_e32 v185, v190
	v_exp_f32_e32 v188, v196
	v_exp_f32_e32 v189, v197
	v_exp_f32_e32 v164, v164
	v_exp_f32_e32 v162, v162
	v_cvt_pk_fp8_f32 v198, v198, v144
	v_cvt_pk_fp8_f32 v199, v199, v150
	v_cvt_pk_fp8_f32 v200, v200, v156
	v_cvt_pk_fp8_f32 v201, v201, v186
	v_cvt_pk_fp8_f32 v202, v202, v145
	v_cvt_pk_fp8_f32 v203, v203, v151
	v_cvt_pk_fp8_f32 v204, v204, v157
	v_cvt_pk_fp8_f32 v205, v205, v187
	s_or_b64 s[0:1], s[0:1], s[42:43]
	v_cvt_pk_fp8_f32 v198, v146, v148 op_sel:[0,0,1]
	v_cvt_pk_fp8_f32 v199, v152, v154 op_sel:[0,0,1]
	v_cvt_pk_fp8_f32 v200, v158, v184 op_sel:[0,0,1]
	v_cvt_pk_fp8_f32 v201, v188, v164 op_sel:[0,0,1]
	v_cvt_pk_fp8_f32 v202, v147, v149 op_sel:[0,0,1]
	v_cvt_pk_fp8_f32 v203, v153, v155 op_sel:[0,0,1]
	v_cvt_pk_fp8_f32 v204, v159, v185 op_sel:[0,0,1]
	v_cvt_pk_fp8_f32 v205, v189, v162 op_sel:[0,0,1]
	s_waitcnt lgkmcnt(0)
	s_and_b64 vcc, exec, s[40:41]
	s_cbranch_vccnz .LBB0_577
	s_mov_b32 m0, s92
	v_lshl_add_u64 v[224:225], s[78:79], 0, v[232:233]
	s_mov_b64 s[6:7], 0x10000
	global_load_lds_dwordx4 v[224:225], off
	v_lshl_add_u64 v[226:227], v[224:225], 0, s[6:7]
	s_mov_b32 m0, s93
	s_mov_b64 s[6:7], 0x30000
	global_load_lds_dwordx4 v[226:227], off
	v_lshl_add_u64 v[226:227], v[224:225], 0, s[26:27]
	s_mov_b32 m0, s94
	s_nop 0
	global_load_lds_dwordx4 v[226:227], off
	v_lshl_add_u64 v[226:227], v[224:225], 0, s[6:7]
	s_mov_b32 m0, s95
	s_mov_b64 s[6:7], 0x40000
	global_load_lds_dwordx4 v[226:227], off
	v_lshl_add_u64 v[226:227], v[224:225], 0, s[6:7]
	s_mov_b32 m0, s96
	s_mov_b64 s[6:7], 0x50000
	global_load_lds_dwordx4 v[226:227], off
	v_lshl_add_u64 v[226:227], v[224:225], 0, s[6:7]
	s_mov_b32 m0, s97
	s_mov_b64 s[6:7], 0x60000
	global_load_lds_dwordx4 v[226:227], off
	v_lshl_add_u64 v[226:227], v[224:225], 0, s[6:7]
	s_mov_b32 m0, s48
	s_mov_b64 s[6:7], 0x70000
	global_load_lds_dwordx4 v[226:227], off
	v_lshl_add_u64 v[224:225], v[224:225], 0, s[6:7]
	s_mov_b32 m0, s49
	s_nop 0
	global_load_lds_dwordx4 v[224:225], off
.LBB0_577:
	v_mfma_f32_32x32x64_f8f6f4 v[48:63], v[198:205], v[104:111], v[48:63]
	s_add_i32 s91, s91, 64
	s_cmp_lg_u32 s23, s88
	v_mfma_f32_32x32x64_f8f6f4 v[64:79], v[198:205], v[96:103], v[64:79]
	v_mfma_f32_32x32x64_f8f6f4 v[32:47], v[198:205], v[120:127], v[32:47]
	v_mfma_f32_32x32x64_f8f6f4 v[0:15], v[198:205], v[112:119], v[0:15]
	v_mfma_f32_32x32x64_f8f6f4 v[16:31], v[198:205], v[208:215], v[16:31]
	s_cbranch_scc0 .LBB0_543
	v_mov_b32_e32 v164, v182
	v_mov_b32_e32 v162, v183
	s_branch .LBB0_555
